# v5 with every workgroup writing back L2 before its barrier arrival (leader write-back removed)
# baseline (speedup 1.0000x reference)
.LBB0_603:
	s_andn2_saveexec_b64 s[10:11], s[10:11]
	s_cbranch_execz .LBB0_621
	s_mov_b64 s[10:11], exec
	s_waitcnt lgkmcnt(0)
	s_waitcnt vmcnt(0)
	v_mbcnt_lo_u32_b32 v2, s10, 0
	v_mbcnt_hi_u32_b32 v2, s11, v2
	v_cmp_eq_u32_e32 vcc, 0, v2
	s_and_saveexec_b64 s[12:13], vcc
	s_cbranch_execz .LBB0_606
	s_bcnt1_i32_b64 s3, s[10:11]
	v_readlane_b32 s16, v253, 2
	v_mov_b32_e32 v3, 0x7000
	v_mov_b32_e32 v4, s3
	v_readlane_b32 s17, v253, 3
	v_readlane_b32 s18, v253, 4
	v_readlane_b32 s19, v253, 5
	s_nop 2
	buffer_wbl2 sc1
	s_waitcnt vmcnt(0)
	global_atomic_add v3, v3, v4, s[16:17] offset:1024 sc0

.LBB0_702:
	s_andn2_saveexec_b64 s[8:9], s[8:9]
	s_cbranch_execz .LBB0_720
	s_mov_b64 s[8:9], exec
	s_waitcnt lgkmcnt(0)
	s_waitcnt vmcnt(0)
	v_mbcnt_lo_u32_b32 v2, s8, 0
	v_mbcnt_hi_u32_b32 v2, s9, v2
	v_cmp_eq_u32_e32 vcc, 0, v2
	s_and_saveexec_b64 s[10:11], vcc
	s_cbranch_execz .LBB0_705
	s_bcnt1_i32_b64 s3, s[8:9]
	v_readlane_b32 s12, v253, 2
	v_mov_b32_e32 v3, 0x7000
	v_mov_b32_e32 v4, s3
	v_readlane_b32 s13, v253, 3
	v_readlane_b32 s14, v253, 4
	v_readlane_b32 s15, v253, 5
	s_nop 2
	buffer_wbl2 sc1
	s_waitcnt vmcnt(0)
	global_atomic_add v3, v3, v4, s[12:13] offset:1024 sc0

.LBB0_781:
	v_readlane_b32 s6, v254, 17
	v_readlane_b32 s7, v254, 18
	v_cvt_f32_u32_e32 v1, v2
	v_sub_u32_e32 v4, 0, v2
	v_rcp_iflag_f32_e32 v1, v1
	s_nop 1
	buffer_wbl2 sc1
	s_waitcnt vmcnt(0)
	global_atomic_add v3, v65, v167, s[6:7] sc0
	v_mul_f32_e32 v1, 0x4f7ffffe, v1
	v_cvt_u32_f32_e32 v1, v1
	v_mul_lo_u32 v4, v4, v1
	v_mul_hi_u32 v4, v1, v4
	v_add_u32_e32 v1, v1, v4
	s_waitcnt vmcnt(0)
	v_mul_hi_u32 v1, v3, v1
	v_mul_lo_u32 v4, v1, v2
	v_sub_u32_e32 v4, v3, v4
	v_add_u32_e32 v5, 1, v1
	v_cmp_ge_u32_e32 vcc, v4, v2
	v_add_u32_e32 v3, 1, v3
	s_nop 0
	v_cndmask_b32_e32 v1, v1, v5, vcc
	v_sub_u32_e32 v5, v4, v2
	v_cndmask_b32_e32 v4, v4, v5, vcc
	v_add_u32_e32 v5, 1, v1
	v_cmp_ge_u32_e32 vcc, v4, v2
	s_nop 1
	v_cndmask_b32_e32 v1, v1, v5, vcc
	v_mul_lo_u32 v4, v2, v1
	v_add_u32_e32 v2, v4, v2
	v_cmp_ne_u32_e32 vcc, v3, v2
	s_and_saveexec_b64 s[6:7], vcc
	s_xor_b64 s[6:7], exec, s[6:7]
	s_cbranch_execz .LBB0_795
	v_readlane_b32 s8, v254, 19
	v_readlane_b32 s9, v254, 20
	s_waitcnt lgkmcnt(0)
	s_nop 3
	global_load_dword v0, v65, s[8:9] sc1
	s_waitcnt vmcnt(0)
	v_cmp_eq_u32_e32 vcc, v0, v1
	s_and_saveexec_b64 s[8:9], vcc
	s_cbranch_execz .LBB0_794
	s_mov_b32 s21, 1
	s_mov_b64 s[10:11], 0
	s_branch .LBB0_785

.LBB0_795:
	s_andn2_saveexec_b64 s[6:7], s[6:7]
	s_cbranch_execz .LBB0_813
	s_mov_b64 s[6:7], exec
	s_waitcnt lgkmcnt(0)
	s_waitcnt vmcnt(0)
	v_mbcnt_lo_u32_b32 v1, s6, 0
	v_mbcnt_hi_u32_b32 v1, s7, v1
	v_cmp_eq_u32_e32 vcc, 0, v1
	s_and_saveexec_b64 s[8:9], vcc
	s_cbranch_execz .LBB0_798
	s_bcnt1_i32_b64 s6, s[6:7]
	v_mov_b32_e32 v2, s6
	v_readlane_b32 s6, v254, 21
	v_readlane_b32 s7, v254, 22
	s_nop 4
	global_atomic_add v2, v65, v2, s[6:7] sc0

.LBB0_2518:
	v_readlane_b32 s6, v254, 17
	v_readlane_b32 s7, v254, 18
	v_cvt_f32_u32_e32 v1, v2
	v_sub_u32_e32 v4, 0, v2
	v_rcp_iflag_f32_e32 v1, v1
	s_nop 1
	buffer_wbl2 sc1
	s_waitcnt vmcnt(0)
	global_atomic_add v3, v65, v167, s[6:7] sc0
	v_mul_f32_e32 v1, 0x4f7ffffe, v1
	v_cvt_u32_f32_e32 v1, v1
	v_mul_lo_u32 v4, v4, v1
	v_mul_hi_u32 v4, v1, v4
	v_add_u32_e32 v1, v1, v4
	s_waitcnt vmcnt(0)
	v_mul_hi_u32 v1, v3, v1
	v_mul_lo_u32 v4, v1, v2
	v_sub_u32_e32 v4, v3, v4
	v_add_u32_e32 v5, 1, v1
	v_cmp_ge_u32_e32 vcc, v4, v2
	v_add_u32_e32 v3, 1, v3
	s_nop 0
	v_cndmask_b32_e32 v1, v1, v5, vcc
	v_sub_u32_e32 v5, v4, v2
	v_cndmask_b32_e32 v4, v4, v5, vcc
	v_add_u32_e32 v5, 1, v1
	v_cmp_ge_u32_e32 vcc, v4, v2
	s_nop 1
	v_cndmask_b32_e32 v1, v1, v5, vcc
	v_mul_lo_u32 v4, v2, v1
	v_add_u32_e32 v2, v4, v2
	v_cmp_ne_u32_e32 vcc, v3, v2
	s_and_saveexec_b64 s[6:7], vcc
	s_xor_b64 s[6:7], exec, s[6:7]
	s_cbranch_execz .LBB0_2532
	v_readlane_b32 s8, v254, 19
	v_readlane_b32 s9, v254, 20
	s_waitcnt lgkmcnt(0)
	s_nop 3
	global_load_dword v0, v65, s[8:9] sc1
	s_waitcnt vmcnt(0)
	v_cmp_eq_u32_e32 vcc, v0, v1
	s_and_saveexec_b64 s[8:9], vcc
	s_cbranch_execz .LBB0_2531
	s_mov_b32 s20, 1
	s_mov_b64 s[10:11], 0
	s_branch .LBB0_2522

.LBB0_2533:
	s_mov_b64 s[6:7], exec
	s_waitcnt lgkmcnt(0)
	s_waitcnt vmcnt(0)
	v_mbcnt_lo_u32_b32 v1, s6, 0
	v_mbcnt_hi_u32_b32 v1, s7, v1
	v_cmp_eq_u32_e32 vcc, 0, v1
	s_and_saveexec_b64 s[8:9], vcc
	s_cbranch_execz .LBB0_2535
	s_bcnt1_i32_b64 s6, s[6:7]
	v_mov_b32_e32 v2, s6
	v_readlane_b32 s6, v254, 21
	v_readlane_b32 s7, v254, 22
	s_nop 4
	global_atomic_add v2, v65, v2, s[6:7] sc0
